# split barrier after the scans: no completion wait after the arrive atomic (wave 0 proceeds to the mixer phase at once)
# baseline (speedup 1.0000x reference)
; #define SEAM() do { if (lo <= ph && ph + 1 < hi) { size_t zb_ = 0; asm volatile("" : "+s"(zb_), "+s"(bar.x)); bar.bar = (unsigned*)(args.ws + WS_CTL + zb_) + CW_BAR; xcd_barrier(bar); } ++ph; } while (0)
; __global__ void __launch_bounds__(NWAVES * 64, 2) mega_fwd(Args args) {
;     ...
;             if (F.wave < 4) { p_scans(F); if (!CV_IN_MIX) p_convert(F, F.l, cv0_, CV_ALL); if (!mixhead_ && F.l + 1 < NLAYER) p_convert(F, F.l + 1, 0, CV_WIN); }
;             else { if (!CV_IN_MIX) p_convert(F, F.l, cv0_, CV_ALL); if (!mixhead_ && F.l + 1 < NLAYER) p_convert(F, F.l + 1, 0, CV_WIN); p_scans(F); } }
;         SEAM();
.LBB0_2163:
	v_readlane_b32 s2, v255, 14
	s_add_i32 s50, s2, 4
	v_readlane_b32 s2, v255, 10
	v_readlane_b32 s3, v255, 11
	s_cmp_lt_i32 s50, s3
	s_cselect_b64 s[2:3], -1, 0
	s_and_b64 s[0:1], s[0:1], s[2:3]
	s_andn2_b64 vcc, exec, s[0:1]
	s_waitcnt vmcnt(0) lgkmcnt(0)
	s_barrier
	s_mov_b64 s[4:5], exec
	v_readlane_b32 s10, v255, 8
	v_readlane_b32 s11, v255, 9
	s_nop 3
	s_and_b64 s[10:11], s[4:5], s[10:11]
	s_mov_b64 exec, s[10:11]
	s_cbranch_execz .Lmy_s4a_done
	buffer_wbl2 sc0 sc1
	s_waitcnt vmcnt(0)
	v_readlane_b32 s12, v255, 5
	v_readlane_b32 s13, v255, 6
	s_nop 3
	v_mov_b32_e32 v0, 0xb000
	v_mov_b32_e32 v1, 1
	global_atomic_add v0, v1, s[12:13]
	s_nop 0
